# mlstm_scan: the sixteen gate loads issued together behind one wait (the last three pairs were serialized behind full vmcnt(0) waits)
# speedup vs baseline: 1.0010x; 1.0010x over previous
.LBB0_158:
	s_lshl_b32 s22, s0, 10
	s_and_b32 s22, s22, 0xfffff000
	s_ashr_i32 s23, s22, 31
	s_and_b32 s1, s0, 3
	s_lshl_b64 s[22:23], s[22:23], 5
	s_add_u32 s22, s48, s22
	s_addc_u32 s23, s49, s23
	s_lshl_b32 s1, s1, 2
	s_add_u32 s22, s22, s1
	s_addc_u32 s23, s23, 0
	v_lshl_add_u64 v[32:33], s[22:23], 0, v[2:3]
	flat_load_dword v31, v[32:33]
	s_nop 0
	flat_load_dword v32, v[32:33] offset:16
	v_lshl_add_u64 v[34:35], s[22:23], 0, v[4:5]
	flat_load_dword v33, v[34:35]
	s_nop 0
	flat_load_dword v34, v[34:35] offset:16
	v_lshl_add_u64 v[36:37], s[22:23], 0, v[6:7]
	flat_load_dword v35, v[36:37]
	s_nop 0
	flat_load_dword v36, v[36:37] offset:16
	v_lshl_add_u64 v[38:39], s[22:23], 0, v[8:9]
	flat_load_dword v37, v[38:39]
	s_nop 0
	flat_load_dword v38, v[38:39] offset:16
	v_lshl_add_u64 v[40:41], s[22:23], 0, v[10:11]
	flat_load_dword v47, v[40:41]
	flat_load_dword v39, v[40:41] offset:16
	v_lshl_add_u64 v[40:41], s[22:23], 0, v[12:13]
	flat_load_dword v49, v[40:41]
	flat_load_dword v66, v[40:41] offset:16
	v_lshl_add_u64 v[40:41], s[22:23], 0, v[14:15]
	flat_load_dword v51, v[40:41]
	flat_load_dword v67, v[40:41] offset:16
	v_lshl_add_u64 v[40:41], s[22:23], 0, v[16:17]
	flat_load_dword v53, v[40:41]
	flat_load_dword v68, v[40:41] offset:16
	s_waitcnt vmcnt(0) lgkmcnt(0)
	v_add_f32_e32 v32, 0, v32
	v_add_f32_e32 v34, v32, v34
	v_add_f32_e32 v36, v34, v36
	v_add_f32_e32 v38, v36, v38
	v_add_f32_e32 v48, v38, v39
	v_add_f32_e32 v50, v48, v66
	v_add_f32_e32 v52, v50, v67
	v_add_f32_e32 v54, v52, v68
	ds_bpermute_b32 v39, v20, v54
	s_waitcnt lgkmcnt(0)
	v_add_f32_e32 v39, v54, v39
	v_cndmask_b32_e32 v39, v39, v54, vcc
	ds_bpermute_b32 v40, v21, v39
	s_waitcnt lgkmcnt(0)
	v_add_f32_e32 v40, v39, v40
	v_cndmask_b32_e64 v39, v40, v39, s[2:3]
	ds_bpermute_b32 v40, v22, v39
	s_waitcnt lgkmcnt(0)
	v_add_f32_e32 v40, v39, v40
	v_cndmask_b32_e64 v39, v40, v39, s[4:5]
	ds_bpermute_b32 v40, v23, v39
	s_waitcnt lgkmcnt(0)
	v_add_f32_e32 v40, v39, v40
	v_cndmask_b32_e64 v39, v40, v39, s[6:7]
	ds_bpermute_b32 v40, v24, v39
	s_waitcnt lgkmcnt(0)
	v_add_f32_e32 v40, v39, v40
	v_cndmask_b32_e64 v39, v40, v39, s[8:9]
	ds_bpermute_b32 v40, v25, v39
	s_waitcnt lgkmcnt(0)
	v_add_f32_e32 v40, v39, v40
	s_and_saveexec_b64 s[22:23], s[12:13]
	ds_write_b32 v27, v40
	s_or_b64 exec, exec, s[22:23]
	v_mov_b32_e32 v41, 0
	s_waitcnt lgkmcnt(0)
	s_barrier
	s_and_saveexec_b64 s[24:25], s[14:15]
	s_cbranch_execz .LBB0_164
	s_mov_b64 s[38:39], 0
	v_mov_b32_e32 v41, 0
	s_mov_b32 s1, s59
	v_mov_b32_e32 v42, v26
